# in2_rowstat_loads_before_kloop_first_iter_copy
# speedup vs baseline: 1.0012x; 1.0011x over previous
; #define PG8_STAGE_A(bufoff, gbase, h, nx) do { if constexpr (GATHER) { unsigned _v[2]; _v[0] = (nx) ? voffAn[h][0] : voffA[h][0]; _v[1] = (nx) ? voffAn[h][1] : voffA[h][1]; PG8_STAGE(bufoff, gbase, _v); } \
;         else PG8_STAGE(bufoff, (gbase) + (h) * hstepA, voffA[0]); } while (0)
; #define PG8_LDA(dst, b, h) do { _Pragma("unroll") for (int m = 0; m < 4; ++m) _Pragma("unroll") for (int k = 0; k < 2; ++k) dst[m][k] = *(const LAS bf16x8*)(lds + PG8_SA(b, h) + aoff + m * 2048 + k * 1024); } while (0)
; #define PG8_LDB(dst, b, h) do { _Pragma("unroll") for (int n = 0; n < 2; ++n) _Pragma("unroll") for (int k = 0; k < 2; ++k) dst[n][k] = *(const LAS bf16x8*)(lds + PG8_SB(b, h) + boff + n * 2048 + k * 1024); } while (0)
; #define PG8_MMA(ai, bj, At, Bt) do { __builtin_amdgcn_s_setprio(1); _Pragma("unroll") for (int m = 0; m < 4; ++m) _Pragma("unroll") for (int n = 0; n < 2; ++n) _Pragma("unroll") for (int k = 0; k < 2; ++k) \
;         acc[ai][bj][m][n] = __builtin_amdgcn_mfma_f32_16x16x32_bf16(Bt[n][k], At[m][k], acc[ai][bj][m][n], 0, 0, 0); __builtin_amdgcn_s_setprio(0); } while (0)
; #define PG8_WAIT_V(n) asm volatile("s_waitcnt vmcnt(" #n ")" ::: "memory")
; #define PG8_WAIT_L(n) asm volatile("s_waitcnt lgkmcnt(" #n ")" ::: "memory")
; #define PG8_BAR __builtin_amdgcn_s_barrier()
; #define PG8_SCHED __builtin_amdgcn_sched_barrier(0)
; template <class Epi, class Sched, bool GATHER, bool ALIGN_EPI>
; __device__ __forceinline__ void gemm_phase(LAS unsigned char* lds, const int wave_, const int K, const int lda, const int ldb, const Sched& S, const Epi& E) {
;     ...
;     f32x4 acc[2][2][4][2];
; #pragma unroll
;     for (int a = 0; a < 2; ++a)
; #pragma unroll
;         for (int b = 0; b < 2; ++b)
; #pragma unroll
;             for (int m = 0; m < 4; ++m)
; #pragma unroll
;                 for (int n = 0; n < 2; ++n) acc[a][b][m][n] = (f32x4){0.f, 0.f, 0.f, 0.f};
;     ...
;             const char* a2 = last ? nA : cA + (size_t)(t + 2) * kstep; const char* b2 = last ? nB : cB + (size_t)(t + 2) * kstep;
;             const char* a3 = a2 + kstep; const char* b3 = b2 + kstep;
;             if (last && has_next) S.a_ready(nxt);
;             PG8_LDB(B0, 0, 0); PG8_LDB(B1, 0, 1); PG8_SCHED; PG8_LDA(At, 0, 0); PG8_STAGE_A(PG8_SA(1, 1), a1, 1, false);
;             PG8_WAIT_V(8); PG8_WAIT_L(0); PG8_BAR; PG8_MMA(0, 0, At, B0); PG8_MMA(0, 1, At, B1); PG8_BAR; PG8_SCHED;
.LBB0_719:
	v_lshl_add_u32 v244, s30, 8, v199
	v_lshlrev_b32_e32 v244, 6, v244
	v_add_u32_e32 v245, 0x2000, v244
	s_add_u32 s4, s4, 0x40080
	s_addc_u32 s5, s5, 0
	s_add_u32 s11, s18, 0x100
	v_mov_b32_e32 v0, 0
	v_mov_b64_e32 v[210:211], 0xff
	s_addc_u32 s13, s19, 0
	s_mov_b32 s31, -2
	v_mov_b32_e32 v1, v0
	v_mov_b32_e32 v2, v0
	v_mov_b32_e32 v3, v0
	v_mov_b32_e32 v4, v0
	v_mov_b32_e32 v5, v0
	v_mov_b32_e32 v6, v0
	v_mov_b32_e32 v7, v0
	v_mov_b32_e32 v16, v0
	v_mov_b32_e32 v17, v0
	v_mov_b32_e32 v18, v0
	v_mov_b32_e32 v19, v0
	v_mov_b32_e32 v20, v0
	v_mov_b32_e32 v21, v0
	v_mov_b32_e32 v22, v0
	v_mov_b32_e32 v23, v0
	v_mov_b32_e32 v32, v0
	v_mov_b32_e32 v33, v0
	v_mov_b32_e32 v34, v0
	v_mov_b32_e32 v35, v0
	v_mov_b32_e32 v36, v0
	v_mov_b32_e32 v37, v0
	v_mov_b32_e32 v38, v0
	v_mov_b32_e32 v39, v0
	v_mov_b32_e32 v48, v0
	v_mov_b32_e32 v49, v0
	v_mov_b32_e32 v50, v0
	v_mov_b32_e32 v51, v0
	v_mov_b32_e32 v52, v0
	v_mov_b32_e32 v53, v0
	v_mov_b32_e32 v54, v0
	v_mov_b32_e32 v55, v0
	v_mov_b32_e32 v8, v0
	v_mov_b32_e32 v9, v0
	v_mov_b32_e32 v10, v0
	v_mov_b32_e32 v11, v0
	v_mov_b32_e32 v12, v0
	v_mov_b32_e32 v13, v0
	v_mov_b32_e32 v14, v0
	v_mov_b32_e32 v15, v0
	v_mov_b32_e32 v24, v0
	v_mov_b32_e32 v25, v0
	v_mov_b32_e32 v26, v0
	v_mov_b32_e32 v27, v0
	v_mov_b32_e32 v28, v0
	v_mov_b32_e32 v29, v0
	v_mov_b32_e32 v30, v0
	v_mov_b32_e32 v31, v0
	v_mov_b32_e32 v40, v0
	v_mov_b32_e32 v41, v0
	v_mov_b32_e32 v42, v0
	v_mov_b32_e32 v43, v0
	v_mov_b32_e32 v44, v0
	v_mov_b32_e32 v45, v0
	v_mov_b32_e32 v46, v0
	v_mov_b32_e32 v47, v0
	v_mov_b32_e32 v56, v0
	v_mov_b32_e32 v57, v0
	v_mov_b32_e32 v58, v0
	v_mov_b32_e32 v59, v0
	v_mov_b32_e32 v60, v0
	v_mov_b32_e32 v61, v0
	v_mov_b32_e32 v62, v0
	v_mov_b32_e32 v63, v0
	v_mov_b32_e32 v64, v0
	v_mov_b32_e32 v65, v0
	v_mov_b32_e32 v66, v0
	v_mov_b32_e32 v67, v0
	v_mov_b32_e32 v68, v0
	v_mov_b32_e32 v69, v0
	v_mov_b32_e32 v70, v0
	v_mov_b32_e32 v71, v0
	v_mov_b32_e32 v80, v0
	v_mov_b32_e32 v81, v0
	v_mov_b32_e32 v82, v0
	v_mov_b32_e32 v83, v0
	v_mov_b32_e32 v84, v0
	v_mov_b32_e32 v85, v0
	v_mov_b32_e32 v86, v0
	v_mov_b32_e32 v87, v0
	v_mov_b32_e32 v96, v0
	v_mov_b32_e32 v97, v0
	v_mov_b32_e32 v98, v0
	v_mov_b32_e32 v99, v0
	v_mov_b32_e32 v100, v0
	v_mov_b32_e32 v101, v0
	v_mov_b32_e32 v102, v0
	v_mov_b32_e32 v103, v0
	v_mov_b32_e32 v112, v0
	v_mov_b32_e32 v113, v0
	v_mov_b32_e32 v114, v0
	v_mov_b32_e32 v115, v0
	v_mov_b32_e32 v116, v0
	v_mov_b32_e32 v117, v0
	v_mov_b32_e32 v118, v0
	v_mov_b32_e32 v119, v0
	v_mov_b32_e32 v72, v0
	v_mov_b32_e32 v73, v0
	v_mov_b32_e32 v74, v0
	v_mov_b32_e32 v75, v0
	v_mov_b32_e32 v76, v0
	v_mov_b32_e32 v77, v0
	v_mov_b32_e32 v78, v0
	v_mov_b32_e32 v79, v0
	v_mov_b32_e32 v88, v0
	v_mov_b32_e32 v89, v0
	v_mov_b32_e32 v90, v0
	v_mov_b32_e32 v91, v0
	v_mov_b32_e32 v92, v0
	v_mov_b32_e32 v93, v0
	v_mov_b32_e32 v94, v0
	v_mov_b32_e32 v95, v0
	v_mov_b32_e32 v104, v0
	v_mov_b32_e32 v105, v0
	v_mov_b32_e32 v106, v0
	v_mov_b32_e32 v107, v0
	v_mov_b32_e32 v108, v0
	v_mov_b32_e32 v109, v0
	v_mov_b32_e32 v110, v0
	v_mov_b32_e32 v111, v0
	v_mov_b32_e32 v120, v0
	v_mov_b32_e32 v121, v0
	v_mov_b32_e32 v122, v0
	v_mov_b32_e32 v123, v0
	v_mov_b32_e32 v124, v0
	v_mov_b32_e32 v125, v0
	v_mov_b32_e32 v126, v0
	v_mov_b32_e32 v127, v0
	global_load_dword v236, v244, s[100:101]
	global_load_dword v237, v244, s[100:101] offset:1024
	global_load_dword v238, v244, s[100:101] offset:2048
	global_load_dword v239, v244, s[100:101] offset:3072
	global_load_dword v240, v245, s[100:101]
	global_load_dword v241, v245, s[100:101] offset:1024
	global_load_dword v242, v245, s[100:101] offset:2048
	global_load_dword v243, v245, s[100:101] offset:3072
	s_add_u32 s2, s4, 0xfffc0080
	s_addc_u32 s3, s5, -1
	s_cmp_eq_u32 s31, 12
	s_cselect_b32 s21, s15, s3
	s_cselect_b32 s20, s14, s2
	s_cselect_b32 s19, s17, s13
	s_cselect_b32 s18, s16, s11
	s_add_i32 s2, 0, 0x10000
	s_add_i32 s8, 0, 0x14000
	v_add_u32_e32 v140, s2, v201
	v_add_u32_e32 v160, s8, v201
	ds_read_b128 v[128:131], v140
	ds_read_b128 v[132:135], v140 offset:1024
	ds_read_b128 v[136:139], v140 offset:2048
	ds_read_b128 v[140:143], v140 offset:3072
	ds_read_b128 v[144:147], v160
	ds_read_b128 v[148:151], v160 offset:1024
	ds_read_b128 v[152:155], v160 offset:2048
	ds_read_b128 v[176:179], v160 offset:3072
	v_lshl_add_u64 v[188:189], s[4:5], 0, v[172:173]
	s_add_i32 m0, s22, 0xc000
	ds_read_b128 v[180:183], v215
	ds_read_b128 v[184:187], v215 offset:1024
	ds_read_b128 v[204:207], v215 offset:2048
	ds_read_b128 v[216:219], v215 offset:3072
	ds_read_b128 v[220:223], v215 offset:4096
	ds_read_b128 v[224:227], v215 offset:5120
	ds_read_b128 v[228:231], v215 offset:6144
	ds_read_b128 v[232:235], v215 offset:7168
	global_load_lds_dwordx4 v[188:189], off
	v_lshl_add_u64 v[188:189], s[4:5], 0, v[174:175]
	s_add_i32 m0, s22, 0xe000
	s_nop 0
	global_load_lds_dwordx4 v[188:189], off
	s_waitcnt vmcnt(16)
	s_waitcnt lgkmcnt(0)
	s_barrier
; #define PG8_STAGE(bufoff, gbase, voff) do { _Pragma("unroll") for (int _i = 0; _i < 2; ++_i) \
;         __builtin_amdgcn_global_load_lds((const unsigned*)((const char*)(gbase) + (voff)[_i]), (LAS unsigned*)(lds + (bufoff) + ldsw + _i * 8192), 16, 0, 0); } while (0)
; #define PG8_STAGE_A(bufoff, gbase, h, nx) do { if constexpr (GATHER) { unsigned _v[2]; _v[0] = (nx) ? voffAn[h][0] : voffA[h][0]; _v[1] = (nx) ? voffAn[h][1] : voffA[h][1]; PG8_STAGE(bufoff, gbase, _v); } \
;         else PG8_STAGE(bufoff, (gbase) + (h) * hstepA, voffA[0]); } while (0)
; #define PG8_LDA(dst, b, h) do { _Pragma("unroll") for (int m = 0; m < 4; ++m) _Pragma("unroll") for (int k = 0; k < 2; ++k) dst[m][k] = *(const LAS bf16x8*)(lds + PG8_SA(b, h) + aoff + m * 2048 + k * 1024); } while (0)
; #define PG8_LDB(dst, b, h) do { _Pragma("unroll") for (int n = 0; n < 2; ++n) _Pragma("unroll") for (int k = 0; k < 2; ++k) dst[n][k] = *(const LAS bf16x8*)(lds + PG8_SB(b, h) + boff + n * 2048 + k * 1024); } while (0)
; #define PG8_MMA(ai, bj, At, Bt) do { __builtin_amdgcn_s_setprio(1); _Pragma("unroll") for (int m = 0; m < 4; ++m) _Pragma("unroll") for (int n = 0; n < 2; ++n) _Pragma("unroll") for (int k = 0; k < 2; ++k) \
;         acc[ai][bj][m][n] = __builtin_amdgcn_mfma_f32_16x16x32_bf16(Bt[n][k], At[m][k], acc[ai][bj][m][n], 0, 0, 0); __builtin_amdgcn_s_setprio(0); } while (0)
; #define PG8_WAIT_V(n) asm volatile("s_waitcnt vmcnt(" #n ")" ::: "memory")
; #define PG8_WAIT_L(n) asm volatile("s_waitcnt lgkmcnt(" #n ")" ::: "memory")
; #define PG8_BAR __builtin_amdgcn_s_barrier()
; #define PG8_SCHED __builtin_amdgcn_sched_barrier(0)
; template <class Epi, class Sched, bool GATHER, bool ALIGN_EPI>
; __device__ __forceinline__ void gemm_phase(LAS unsigned char* lds, const int wave_, const int K, const int lda, const int ldb, const Sched& S, const Epi& E) {
;     ...
;             PG8_LDB(B0, 0, 0); PG8_LDB(B1, 0, 1); PG8_SCHED; PG8_LDA(At, 0, 0); PG8_STAGE_A(PG8_SA(1, 1), a1, 1, false);
;             PG8_WAIT_V(8); PG8_WAIT_L(0); PG8_BAR; PG8_MMA(0, 0, At, B0); PG8_MMA(0, 1, At, B1); PG8_BAR; PG8_SCHED;
;             PG8_LDA(At, 0, 1); PG8_STAGE(PG8_SB(0, 0), b2, voffB); PG8_STAGE(PG8_SB(0, 1), b2 + hstepB, voffB); PG8_STAGE_A(PG8_SA(0, 0), a2, 0, last);
;             PG8_WAIT_V(8); PG8_WAIT_L(0); PG8_BAR; PG8_MMA(1, 0, At, B0); PG8_MMA(1, 1, At, B1); PG8_BAR; PG8_SCHED;
	s_setprio 1
	s_waitcnt lgkmcnt(0)
	v_mfma_f32_16x16x32_bf16 v[124:127], v[128:131], v[180:183], v[124:127]
	v_mfma_f32_16x16x32_bf16 v[120:123], v[136:139], v[180:183], v[120:123]
	v_mfma_f32_16x16x32_bf16 v[108:111], v[128:131], v[204:207], v[108:111]
	v_mfma_f32_16x16x32_bf16 v[104:107], v[136:139], v[204:207], v[104:107]
	v_mfma_f32_16x16x32_bf16 v[92:95], v[128:131], v[220:223], v[92:95]
	v_mfma_f32_16x16x32_bf16 v[88:91], v[136:139], v[220:223], v[88:91]
	v_mfma_f32_16x16x32_bf16 v[76:79], v[128:131], v[228:231], v[76:79]
	v_mfma_f32_16x16x32_bf16 v[72:75], v[136:139], v[228:231], v[72:75]
	v_mfma_f32_16x16x32_bf16 v[124:127], v[132:135], v[184:187], v[124:127]
	v_mfma_f32_16x16x32_bf16 v[120:123], v[140:143], v[184:187], v[120:123]
	v_mfma_f32_16x16x32_bf16 v[108:111], v[132:135], v[216:219], v[108:111]
	v_mfma_f32_16x16x32_bf16 v[104:107], v[140:143], v[216:219], v[104:107]
	v_mfma_f32_16x16x32_bf16 v[92:95], v[132:135], v[224:227], v[92:95]
	v_mfma_f32_16x16x32_bf16 v[88:91], v[140:143], v[224:227], v[88:91]
	v_mfma_f32_16x16x32_bf16 v[76:79], v[132:135], v[232:235], v[76:79]
	v_mfma_f32_16x16x32_bf16 v[72:75], v[140:143], v[232:235], v[72:75]
	s_setprio 0
	s_setprio 1
	v_mfma_f32_16x16x32_bf16 v[116:119], v[144:147], v[180:183], v[116:119]
	v_mfma_f32_16x16x32_bf16 v[112:115], v[152:155], v[180:183], v[112:115]
	v_mfma_f32_16x16x32_bf16 v[100:103], v[144:147], v[204:207], v[100:103]
	v_mfma_f32_16x16x32_bf16 v[96:99], v[152:155], v[204:207], v[96:99]
	v_mfma_f32_16x16x32_bf16 v[84:87], v[144:147], v[220:223], v[84:87]
	v_mfma_f32_16x16x32_bf16 v[80:83], v[152:155], v[220:223], v[80:83]
	v_mfma_f32_16x16x32_bf16 v[68:71], v[144:147], v[228:231], v[68:71]
	v_mfma_f32_16x16x32_bf16 v[64:67], v[152:155], v[228:231], v[64:67]
	v_mfma_f32_16x16x32_bf16 v[116:119], v[148:151], v[184:187], v[116:119]
	v_mfma_f32_16x16x32_bf16 v[112:115], v[176:179], v[184:187], v[112:115]
	v_mfma_f32_16x16x32_bf16 v[100:103], v[148:151], v[216:219], v[100:103]
	v_mfma_f32_16x16x32_bf16 v[96:99], v[176:179], v[216:219], v[96:99]
	v_mfma_f32_16x16x32_bf16 v[84:87], v[148:151], v[224:227], v[84:87]
	v_mfma_f32_16x16x32_bf16 v[80:83], v[176:179], v[224:227], v[80:83]
	v_mfma_f32_16x16x32_bf16 v[68:71], v[148:151], v[232:235], v[68:71]
	v_mfma_f32_16x16x32_bf16 v[64:67], v[176:179], v[232:235], v[64:67]
	s_setprio 0
	s_barrier
	s_add_i32 s2, s2, s62
	v_lshl_add_u64 v[188:189], s[18:19], 0, v[156:157]
	s_mov_b32 m0, s2
	ds_read_b128 v[180:183], v215 offset:16384
	ds_read_b128 v[184:187], v215 offset:17408
	ds_read_b128 v[204:207], v215 offset:18432
	ds_read_b128 v[216:219], v215 offset:19456
	ds_read_b128 v[220:223], v215 offset:20480
	ds_read_b128 v[224:227], v215 offset:21504
	ds_read_b128 v[228:231], v215 offset:22528
	ds_read_b128 v[232:235], v215 offset:23552
	global_load_lds_dwordx4 v[188:189], off
	s_add_i32 m0, s2, 0x2000
	s_add_u32 s2, s18, 0x40000
	v_lshl_add_u64 v[190:191], s[18:19], 0, v[162:163]
	s_addc_u32 s3, s19, 0
	s_add_i32 s8, s8, s62
	global_load_lds_dwordx4 v[190:191], off
	v_lshl_add_u64 v[192:193], s[2:3], 0, v[156:157]
	s_mov_b32 m0, s8
	v_lshl_add_u64 v[196:197], s[20:21], 0, v[164:165]
	global_load_lds_dwordx4 v[192:193], off
	v_lshl_add_u64 v[192:193], s[2:3], 0, v[162:163]
	s_add_i32 m0, s8, 0x2000
	s_nop 0
	global_load_lds_dwordx4 v[192:193], off
	v_lshl_add_u64 v[192:193], s[20:21], 0, v[158:159]
	s_mov_b32 m0, s22
	s_nop 0
	global_load_lds_dwordx4 v[192:193], off
	s_mov_b32 m0, s23
	s_nop 0
	global_load_lds_dwordx4 v[196:197], off
	s_waitcnt vmcnt(16)
	s_waitcnt lgkmcnt(0)
	s_barrier
	s_setprio 1
	s_waitcnt lgkmcnt(0)
	v_mfma_f32_16x16x32_bf16 v[60:63], v[128:131], v[180:183], v[60:63]
	v_mfma_f32_16x16x32_bf16 v[56:59], v[136:139], v[180:183], v[56:59]
	v_mfma_f32_16x16x32_bf16 v[44:47], v[128:131], v[204:207], v[44:47]
	v_mfma_f32_16x16x32_bf16 v[40:43], v[136:139], v[204:207], v[40:43]
	v_mfma_f32_16x16x32_bf16 v[28:31], v[128:131], v[220:223], v[28:31]
	v_mfma_f32_16x16x32_bf16 v[24:27], v[136:139], v[220:223], v[24:27]
	v_mfma_f32_16x16x32_bf16 v[12:15], v[128:131], v[228:231], v[12:15]
	v_mfma_f32_16x16x32_bf16 v[8:11], v[136:139], v[228:231], v[8:11]
	v_mfma_f32_16x16x32_bf16 v[60:63], v[132:135], v[184:187], v[60:63]
	v_mfma_f32_16x16x32_bf16 v[56:59], v[140:143], v[184:187], v[56:59]
	v_mfma_f32_16x16x32_bf16 v[44:47], v[132:135], v[216:219], v[44:47]
	v_mfma_f32_16x16x32_bf16 v[40:43], v[140:143], v[216:219], v[40:43]
	v_mfma_f32_16x16x32_bf16 v[28:31], v[132:135], v[224:227], v[28:31]
	v_mfma_f32_16x16x32_bf16 v[24:27], v[140:143], v[224:227], v[24:27]
	v_mfma_f32_16x16x32_bf16 v[12:15], v[132:135], v[232:235], v[12:15]
	v_mfma_f32_16x16x32_bf16 v[8:11], v[140:143], v[232:235], v[8:11]
	s_setprio 0
	s_setprio 1
	v_mfma_f32_16x16x32_bf16 v[52:55], v[144:147], v[180:183], v[52:55]
	v_mfma_f32_16x16x32_bf16 v[48:51], v[152:155], v[180:183], v[48:51]
	v_mfma_f32_16x16x32_bf16 v[36:39], v[144:147], v[204:207], v[36:39]
	v_mfma_f32_16x16x32_bf16 v[32:35], v[152:155], v[204:207], v[32:35]
	v_mfma_f32_16x16x32_bf16 v[20:23], v[144:147], v[220:223], v[20:23]
	v_mfma_f32_16x16x32_bf16 v[16:19], v[152:155], v[220:223], v[16:19]
	v_mfma_f32_16x16x32_bf16 v[4:7], v[144:147], v[228:231], v[4:7]
	v_mfma_f32_16x16x32_bf16 v[0:3], v[152:155], v[228:231], v[0:3]
	v_mfma_f32_16x16x32_bf16 v[52:55], v[148:151], v[184:187], v[52:55]
	v_mfma_f32_16x16x32_bf16 v[48:51], v[176:179], v[184:187], v[48:51]
	v_mfma_f32_16x16x32_bf16 v[36:39], v[148:151], v[216:219], v[36:39]
	v_mfma_f32_16x16x32_bf16 v[32:35], v[176:179], v[216:219], v[32:35]
	v_mfma_f32_16x16x32_bf16 v[20:23], v[148:151], v[224:227], v[20:23]
	v_mfma_f32_16x16x32_bf16 v[16:19], v[176:179], v[224:227], v[16:19]
	v_mfma_f32_16x16x32_bf16 v[4:7], v[148:151], v[232:235], v[4:7]
	v_mfma_f32_16x16x32_bf16 v[0:3], v[176:179], v[232:235], v[0:3]
	s_setprio 0
	s_barrier
; #define PG8_STAGE_A(bufoff, gbase, h, nx) do { if constexpr (GATHER) { unsigned _v[2]; _v[0] = (nx) ? voffAn[h][0] : voffA[h][0]; _v[1] = (nx) ? voffAn[h][1] : voffA[h][1]; PG8_STAGE(bufoff, gbase, _v); } \
;         else PG8_STAGE(bufoff, (gbase) + (h) * hstepA, voffA[0]); } while (0)
; #define PG8_LDA(dst, b, h) do { _Pragma("unroll") for (int m = 0; m < 4; ++m) _Pragma("unroll") for (int k = 0; k < 2; ++k) dst[m][k] = *(const LAS bf16x8*)(lds + PG8_SA(b, h) + aoff + m * 2048 + k * 1024); } while (0)
; #define PG8_LDB(dst, b, h) do { _Pragma("unroll") for (int n = 0; n < 2; ++n) _Pragma("unroll") for (int k = 0; k < 2; ++k) dst[n][k] = *(const LAS bf16x8*)(lds + PG8_SB(b, h) + boff + n * 2048 + k * 1024); } while (0)
; #define PG8_MMA(ai, bj, At, Bt) do { __builtin_amdgcn_s_setprio(1); _Pragma("unroll") for (int m = 0; m < 4; ++m) _Pragma("unroll") for (int n = 0; n < 2; ++n) _Pragma("unroll") for (int k = 0; k < 2; ++k) \
;         acc[ai][bj][m][n] = __builtin_amdgcn_mfma_f32_16x16x32_bf16(Bt[n][k], At[m][k], acc[ai][bj][m][n], 0, 0, 0); __builtin_amdgcn_s_setprio(0); } while (0)
; #define PG8_WAIT_V(n) asm volatile("s_waitcnt vmcnt(" #n ")" ::: "memory")
; #define PG8_WAIT_L(n) asm volatile("s_waitcnt lgkmcnt(" #n ")" ::: "memory")
; #define PG8_BAR __builtin_amdgcn_s_barrier()
; #define PG8_SCHED __builtin_amdgcn_sched_barrier(0)
; template <class Epi, class Sched, bool GATHER, bool ALIGN_EPI>
; __device__ __forceinline__ void gemm_phase(LAS unsigned char* lds, const int wave_, const int K, const int lda, const int ldb, const Sched& S, const Epi& E) {
;     ...
;             PG8_LDB(B0, 1, 0); PG8_LDB(B1, 1, 1); PG8_SCHED; PG8_LDA(At, 1, 0); PG8_STAGE_A(PG8_SA(0, 1), a2, 1, last);
;             PG8_WAIT_V(8); PG8_WAIT_L(0); PG8_BAR; PG8_MMA(0, 0, At, B0); PG8_MMA(0, 1, At, B1); PG8_BAR; PG8_SCHED;
	s_add_i32 s8, 0, 0x18000
	s_add_i32 s9, 0, 0x1c000
	v_add_u32_e32 v140, s8, v201
	v_add_u32_e32 v160, s9, v201
	ds_read_b128 v[128:131], v140
	ds_read_b128 v[132:135], v140 offset:1024
	ds_read_b128 v[136:139], v140 offset:2048
	ds_read_b128 v[140:143], v140 offset:3072
	ds_read_b128 v[144:147], v160
	ds_read_b128 v[148:151], v160 offset:1024
	ds_read_b128 v[152:155], v160 offset:2048
	ds_read_b128 v[176:179], v160 offset:3072
	s_add_u32 s2, s20, 0x40000
	s_addc_u32 s3, s21, 0
	s_mov_b32 m0, s24
	v_lshl_add_u64 v[208:209], s[2:3], 0, v[158:159]
	ds_read_b128 v[180:183], v215 offset:32768
	ds_read_b128 v[184:187], v215 offset:33792
	ds_read_b128 v[204:207], v215 offset:34816
	ds_read_b128 v[216:219], v215 offset:35840
	ds_read_b128 v[220:223], v215 offset:36864
	ds_read_b128 v[224:227], v215 offset:37888
	ds_read_b128 v[228:231], v215 offset:38912
	ds_read_b128 v[232:235], v215 offset:39936
	global_load_lds_dwordx4 v[208:209], off
	v_lshl_add_u64 v[208:209], s[2:3], 0, v[164:165]
	s_mov_b32 m0, s25
	s_nop 0
	global_load_lds_dwordx4 v[208:209], off
	s_waitcnt vmcnt(16)
	s_waitcnt lgkmcnt(0)
	s_barrier
	s_setprio 1
	s_waitcnt lgkmcnt(0)
	v_mfma_f32_16x16x32_bf16 v[124:127], v[128:131], v[180:183], v[124:127]
	v_mfma_f32_16x16x32_bf16 v[120:123], v[136:139], v[180:183], v[120:123]
	v_mfma_f32_16x16x32_bf16 v[108:111], v[128:131], v[204:207], v[108:111]
	v_mfma_f32_16x16x32_bf16 v[104:107], v[136:139], v[204:207], v[104:107]
	v_mfma_f32_16x16x32_bf16 v[92:95], v[128:131], v[220:223], v[92:95]
	v_mfma_f32_16x16x32_bf16 v[88:91], v[136:139], v[220:223], v[88:91]
	v_mfma_f32_16x16x32_bf16 v[76:79], v[128:131], v[228:231], v[76:79]
	v_mfma_f32_16x16x32_bf16 v[72:75], v[136:139], v[228:231], v[72:75]
	v_mfma_f32_16x16x32_bf16 v[124:127], v[132:135], v[184:187], v[124:127]
	v_mfma_f32_16x16x32_bf16 v[120:123], v[140:143], v[184:187], v[120:123]
	v_mfma_f32_16x16x32_bf16 v[108:111], v[132:135], v[216:219], v[108:111]
	v_mfma_f32_16x16x32_bf16 v[104:107], v[140:143], v[216:219], v[104:107]
	v_mfma_f32_16x16x32_bf16 v[92:95], v[132:135], v[224:227], v[92:95]
	v_mfma_f32_16x16x32_bf16 v[88:91], v[140:143], v[224:227], v[88:91]
	v_mfma_f32_16x16x32_bf16 v[76:79], v[132:135], v[232:235], v[76:79]
	v_mfma_f32_16x16x32_bf16 v[72:75], v[140:143], v[232:235], v[72:75]
	s_setprio 0
	s_setprio 1
	v_mfma_f32_16x16x32_bf16 v[116:119], v[144:147], v[180:183], v[116:119]
	v_mfma_f32_16x16x32_bf16 v[112:115], v[152:155], v[180:183], v[112:115]
	v_mfma_f32_16x16x32_bf16 v[100:103], v[144:147], v[204:207], v[100:103]
	v_mfma_f32_16x16x32_bf16 v[96:99], v[152:155], v[204:207], v[96:99]
	v_mfma_f32_16x16x32_bf16 v[84:87], v[144:147], v[220:223], v[84:87]
	v_mfma_f32_16x16x32_bf16 v[80:83], v[152:155], v[220:223], v[80:83]
	v_mfma_f32_16x16x32_bf16 v[68:71], v[144:147], v[228:231], v[68:71]
	v_mfma_f32_16x16x32_bf16 v[64:67], v[152:155], v[228:231], v[64:67]
	v_mfma_f32_16x16x32_bf16 v[116:119], v[148:151], v[184:187], v[116:119]
	v_mfma_f32_16x16x32_bf16 v[112:115], v[176:179], v[184:187], v[112:115]
	v_mfma_f32_16x16x32_bf16 v[100:103], v[148:151], v[216:219], v[100:103]
	v_mfma_f32_16x16x32_bf16 v[96:99], v[176:179], v[216:219], v[96:99]
	v_mfma_f32_16x16x32_bf16 v[84:87], v[148:151], v[224:227], v[84:87]
	v_mfma_f32_16x16x32_bf16 v[80:83], v[176:179], v[224:227], v[80:83]
	v_mfma_f32_16x16x32_bf16 v[68:71], v[148:151], v[232:235], v[68:71]
	v_mfma_f32_16x16x32_bf16 v[64:67], v[176:179], v[232:235], v[64:67]
	s_setprio 0
	s_barrier
; #define PG8_STAGE(bufoff, gbase, voff) do { _Pragma("unroll") for (int _i = 0; _i < 2; ++_i) \
;         __builtin_amdgcn_global_load_lds((const unsigned*)((const char*)(gbase) + (voff)[_i]), (LAS unsigned*)(lds + (bufoff) + ldsw + _i * 8192), 16, 0, 0); } while (0)
; #define PG8_STAGE_A(bufoff, gbase, h, nx) do { if constexpr (GATHER) { unsigned _v[2]; _v[0] = (nx) ? voffAn[h][0] : voffA[h][0]; _v[1] = (nx) ? voffAn[h][1] : voffA[h][1]; PG8_STAGE(bufoff, gbase, _v); } \
;         else PG8_STAGE(bufoff, (gbase) + (h) * hstepA, voffA[0]); } while (0)
; #define PG8_LDA(dst, b, h) do { _Pragma("unroll") for (int m = 0; m < 4; ++m) _Pragma("unroll") for (int k = 0; k < 2; ++k) dst[m][k] = *(const LAS bf16x8*)(lds + PG8_SA(b, h) + aoff + m * 2048 + k * 1024); } while (0)
; #define PG8_MMA(ai, bj, At, Bt) do { __builtin_amdgcn_s_setprio(1); _Pragma("unroll") for (int m = 0; m < 4; ++m) _Pragma("unroll") for (int n = 0; n < 2; ++n) _Pragma("unroll") for (int k = 0; k < 2; ++k) \
;         acc[ai][bj][m][n] = __builtin_amdgcn_mfma_f32_16x16x32_bf16(Bt[n][k], At[m][k], acc[ai][bj][m][n], 0, 0, 0); __builtin_amdgcn_s_setprio(0); } while (0)
; #define PG8_WAIT_V(n) asm volatile("s_waitcnt vmcnt(" #n ")" ::: "memory")
; #define PG8_WAIT_L(n) asm volatile("s_waitcnt lgkmcnt(" #n ")" ::: "memory")
; #define PG8_BAR __builtin_amdgcn_s_barrier()
; #define PG8_SCHED __builtin_amdgcn_sched_barrier(0)
; template <class Epi, class Sched, bool GATHER, bool ALIGN_EPI>
; __device__ __forceinline__ void gemm_phase(LAS unsigned char* lds, const int wave_, const int K, const int lda, const int ldb, const Sched& S, const Epi& E) {
;     ...
;         for (int t = 0; t < nt; t += 2) {
;             const bool last = (t == nt - 2);
;             const char* a1 = cA + (size_t)(t + 1) * kstep;
;             const char* a2 = last ? nA : cA + (size_t)(t + 2) * kstep; const char* b2 = last ? nB : cB + (size_t)(t + 2) * kstep;
;             const char* a3 = a2 + kstep; const char* b3 = b2 + kstep;
;     ...
;             PG8_LDA(At, 1, 1); PG8_STAGE(PG8_SB(1, 0), b3, voffB); PG8_STAGE(PG8_SB(1, 1), b3 + hstepB, voffB); PG8_STAGE_A(PG8_SA(1, 0), a3, 0, last);
;             PG8_WAIT_V(8); PG8_WAIT_L(0); PG8_BAR; PG8_MMA(1, 0, At, B0); PG8_MMA(1, 1, At, B1); PG8_BAR; PG8_SCHED;
	s_add_i32 s2, s8, s62
	v_lshl_add_u64 v[188:189], v[188:189], 0, s[68:69]
	s_mov_b32 m0, s2
	ds_read_b128 v[180:183], v215 offset:49152
	ds_read_b128 v[184:187], v215 offset:50176
	ds_read_b128 v[204:207], v215 offset:51200
	ds_read_b128 v[216:219], v215 offset:52224
	ds_read_b128 v[220:223], v215 offset:53248
	ds_read_b128 v[224:227], v215 offset:54272
	ds_read_b128 v[228:231], v215 offset:55296
	ds_read_b128 v[232:235], v215 offset:56320
	global_load_lds_dwordx4 v[188:189], off
	s_add_i32 m0, s2, 0x2000
	s_add_u32 s2, s18, 0x40080
	v_lshl_add_u64 v[188:189], v[190:191], 0, s[68:69]
	s_addc_u32 s3, s19, 0
	s_add_i32 s8, s9, s62
	global_load_lds_dwordx4 v[188:189], off
	v_lshl_add_u64 v[188:189], s[2:3], 0, v[156:157]
	s_mov_b32 m0, s8
	s_nop 0
	global_load_lds_dwordx4 v[188:189], off
	v_lshl_add_u64 v[188:189], s[2:3], 0, v[162:163]
	s_add_i32 m0, s8, 0x2000
	s_nop 0
	global_load_lds_dwordx4 v[188:189], off
	v_lshl_add_u64 v[188:189], v[192:193], 0, s[68:69]
	s_mov_b32 m0, s26
	s_nop 0
	global_load_lds_dwordx4 v[188:189], off
	v_lshl_add_u64 v[188:189], v[196:197], 0, s[68:69]
	s_mov_b32 m0, s27
	s_nop 0
	global_load_lds_dwordx4 v[188:189], off
	s_waitcnt vmcnt(16)
	s_waitcnt lgkmcnt(0)
	s_barrier
	s_setprio 1
	s_waitcnt lgkmcnt(0)
	v_mfma_f32_16x16x32_bf16 v[60:63], v[128:131], v[180:183], v[60:63]
	v_mfma_f32_16x16x32_bf16 v[56:59], v[136:139], v[180:183], v[56:59]
	v_mfma_f32_16x16x32_bf16 v[44:47], v[128:131], v[204:207], v[44:47]
	v_mfma_f32_16x16x32_bf16 v[40:43], v[136:139], v[204:207], v[40:43]
	v_mfma_f32_16x16x32_bf16 v[28:31], v[128:131], v[220:223], v[28:31]
	v_mfma_f32_16x16x32_bf16 v[24:27], v[136:139], v[220:223], v[24:27]
	v_mfma_f32_16x16x32_bf16 v[12:15], v[128:131], v[228:231], v[12:15]
	v_mfma_f32_16x16x32_bf16 v[8:11], v[136:139], v[228:231], v[8:11]
	v_mfma_f32_16x16x32_bf16 v[60:63], v[132:135], v[184:187], v[60:63]
	v_mfma_f32_16x16x32_bf16 v[56:59], v[140:143], v[184:187], v[56:59]
	v_mfma_f32_16x16x32_bf16 v[44:47], v[132:135], v[216:219], v[44:47]
	v_mfma_f32_16x16x32_bf16 v[40:43], v[140:143], v[216:219], v[40:43]
	v_mfma_f32_16x16x32_bf16 v[28:31], v[132:135], v[224:227], v[28:31]
	v_mfma_f32_16x16x32_bf16 v[24:27], v[140:143], v[224:227], v[24:27]
	v_mfma_f32_16x16x32_bf16 v[12:15], v[132:135], v[232:235], v[12:15]
	v_mfma_f32_16x16x32_bf16 v[8:11], v[140:143], v[232:235], v[8:11]
	s_setprio 0
	s_setprio 1
	v_mfma_f32_16x16x32_bf16 v[52:55], v[144:147], v[180:183], v[52:55]
	v_mfma_f32_16x16x32_bf16 v[48:51], v[152:155], v[180:183], v[48:51]
	v_mfma_f32_16x16x32_bf16 v[36:39], v[144:147], v[204:207], v[36:39]
	v_mfma_f32_16x16x32_bf16 v[32:35], v[152:155], v[204:207], v[32:35]
	v_mfma_f32_16x16x32_bf16 v[20:23], v[144:147], v[220:223], v[20:23]
	v_mfma_f32_16x16x32_bf16 v[16:19], v[152:155], v[220:223], v[16:19]
	v_mfma_f32_16x16x32_bf16 v[4:7], v[144:147], v[228:231], v[4:7]
	v_mfma_f32_16x16x32_bf16 v[0:3], v[152:155], v[228:231], v[0:3]
	v_mfma_f32_16x16x32_bf16 v[52:55], v[148:151], v[184:187], v[52:55]
	v_mfma_f32_16x16x32_bf16 v[48:51], v[176:179], v[184:187], v[48:51]
	v_mfma_f32_16x16x32_bf16 v[36:39], v[148:151], v[216:219], v[36:39]
	v_mfma_f32_16x16x32_bf16 v[32:35], v[176:179], v[216:219], v[32:35]
	v_mfma_f32_16x16x32_bf16 v[20:23], v[148:151], v[224:227], v[20:23]
	v_mfma_f32_16x16x32_bf16 v[16:19], v[176:179], v[224:227], v[16:19]
	v_mfma_f32_16x16x32_bf16 v[4:7], v[148:151], v[232:235], v[4:7]
	v_mfma_f32_16x16x32_bf16 v[0:3], v[176:179], v[232:235], v[0:3]
	s_setprio 0
	s_barrier
	s_add_i32 s31, s31, 2
	s_add_u32 s4, s4, 0x100
	s_addc_u32 s5, s5, 0
	s_add_u32 s11, s11, 0x100
	s_addc_u32 s13, s13, 0
	s_cmp_gt_u32 s31, 13

; template <int M> __device__ __forceinline__ float swz_xor(float v) { return __int_as_float(__builtin_amdgcn_ds_swizzle(__float_as_int(v), (M << 10) | 0x1f)); }
; __device__ __forceinline__ float half_sum(float v) { auto rr = __builtin_amdgcn_permlane32_swap(__float_as_uint(v), __float_as_uint(v), false, false); return __uint_as_float(rr[0]) + __uint_as_float(rr[1]); }
; __device__ __forceinline__ void row_rscale8(const float* part, const int (&rows)[2][4], int fq, float (&rs)[2][4]) {
;     ...
;         for (int m = 0; m < 4; ++m) { float s = (v[ai][m][0] + v[ai][m][1]) + (v[ai][m][2] + v[ai][m][3]); s += swz_xor<16>(s); s = half_sum(s); rs[ai][m] = __builtin_amdgcn_rcpf(sqrtf(s * (1.0f / DM) + EPS)); }
;     __device__ __forceinline__ bool operator()(f32x4 (&acc)[2][2][4][2], const pg8::Unit& u, int wr, int wc, int fr, int fq) const {
;         const int pn = u.pn, row0 = u.pm * 256 + wr * 64 + fr;
;         float rs_[2][4]; { int rows_[2][4];
; #pragma unroll
;             for (int ai = 0; ai < 2; ++ai)
; #pragma unroll
;                 for (int m = 0; m < 4; ++m) rows_[ai][m] = row0 + ai * 128 + m * 16;
;             row_rscale8(part, rows_, fq, rs_); }
.LBB0_723:
	v_lshl_add_u32 v184, s30, 8, v199
	v_ashrrev_i32_e32 v185, 31, v184
	v_or_b32_e32 v196, 16, v184
	v_ashrrev_i32_e32 v197, 31, v196
	v_or_b32_e32 v188, 32, v184
	v_ashrrev_i32_e32 v189, 31, v188
	v_or_b32_e32 v186, 48, v184
	v_ashrrev_i32_e32 v187, 31, v186
	v_add_u32_e32 v182, 0x80, v184
	v_ashrrev_i32_e32 v183, 31, v182
	v_add_u32_e32 v180, 0x90, v184
	v_ashrrev_i32_e32 v181, 31, v180
	v_add_u32_e32 v178, 0xa0, v184
	v_ashrrev_i32_e32 v179, 31, v178
	s_mov_b32 s2, 0xf800000
	v_add_u32_e32 v176, 0xb0, v184
	v_ashrrev_i32_e32 v177, 31, v176
	s_cmp_gt_i32 s29, 7
	v_mov_b64_e32 v[230:231], v[210:211]
	v_fmamk_f32 v160, v236, 0x3a800000, v212
	v_cmp_gt_f32_e32 vcc, s2, v160
	v_mul_f32_e32 v190, 0x4f800000, v160
	s_nop 0
	v_cndmask_b32_e32 v160, v160, v190, vcc
	v_sqrt_f32_e32 v190, v160
	s_nop 0
	v_add_u32_e32 v191, -1, v190
	v_fma_f32 v192, -v191, v190, v160
	v_cmp_ge_f32_e64 s[4:5], 0, v192
	v_add_u32_e32 v192, 1, v190
	s_nop 0
	v_cndmask_b32_e64 v191, v190, v191, s[4:5]
	v_fma_f32 v190, -v192, v190, v160
	v_cmp_lt_f32_e64 s[4:5], 0, v190
	s_nop 1
	v_cndmask_b32_e64 v190, v191, v192, s[4:5]
	v_mul_f32_e32 v191, 0x37800000, v190
	v_cndmask_b32_e32 v190, v190, v191, vcc
	v_cmp_class_f32_e32 vcc, v160, v248
	v_fmamk_f32 v152, v237, 0x3a800000, v212
	v_mul_f32_e32 v153, 0x4f800000, v152
	v_cndmask_b32_e32 v160, v190, v160, vcc
	v_cmp_gt_f32_e32 vcc, s2, v152
	s_nop 1
	v_cndmask_b32_e32 v152, v152, v153, vcc
	v_sqrt_f32_e32 v153, v152
	s_nop 0
	v_add_u32_e32 v154, -1, v153
	v_fma_f32 v155, -v154, v153, v152
	v_cmp_ge_f32_e64 s[4:5], 0, v155
	v_add_u32_e32 v155, 1, v153
	s_nop 0
	v_cndmask_b32_e64 v154, v153, v154, s[4:5]
	v_fma_f32 v153, -v155, v153, v152
	v_cmp_lt_f32_e64 s[4:5], 0, v153
	s_nop 1
	v_cndmask_b32_e64 v153, v154, v155, s[4:5]
	v_mul_f32_e32 v154, 0x37800000, v153
	v_cndmask_b32_e32 v153, v153, v154, vcc
	v_cmp_class_f32_e32 vcc, v152, v248
	v_fmamk_f32 v148, v238, 0x3a800000, v212
	v_mul_f32_e32 v149, 0x4f800000, v148
	v_cndmask_b32_e32 v152, v153, v152, vcc
	v_cmp_gt_f32_e32 vcc, s2, v148
	s_nop 1
	v_cndmask_b32_e32 v148, v148, v149, vcc
	v_sqrt_f32_e32 v149, v148
	s_nop 0
	v_add_u32_e32 v150, -1, v149
	v_fma_f32 v151, -v150, v149, v148
	v_cmp_ge_f32_e64 s[4:5], 0, v151
	v_add_u32_e32 v151, 1, v149
	s_nop 0
	v_cndmask_b32_e64 v150, v149, v150, s[4:5]
	v_fma_f32 v149, -v151, v149, v148
	v_cmp_lt_f32_e64 s[4:5], 0, v149
	s_nop 1
	v_cndmask_b32_e64 v149, v150, v151, s[4:5]
	v_mul_f32_e32 v150, 0x37800000, v149
	v_cndmask_b32_e32 v149, v149, v150, vcc
	v_cmp_class_f32_e32 vcc, v148, v248
	v_fmamk_f32 v144, v239, 0x3a800000, v212
	v_mul_f32_e32 v145, 0x4f800000, v144
	v_cndmask_b32_e32 v148, v149, v148, vcc
	v_cmp_gt_f32_e32 vcc, s2, v144
	s_nop 1
	v_cndmask_b32_e32 v144, v144, v145, vcc
	v_sqrt_f32_e32 v145, v144
	s_nop 0
	v_add_u32_e32 v146, -1, v145
	v_fma_f32 v147, -v146, v145, v144
	v_cmp_ge_f32_e64 s[4:5], 0, v147
	v_add_u32_e32 v147, 1, v145
	s_nop 0
	v_cndmask_b32_e64 v146, v145, v146, s[4:5]
	v_fma_f32 v145, -v147, v145, v144
	v_cmp_lt_f32_e64 s[4:5], 0, v145
	s_nop 1
	v_cndmask_b32_e64 v145, v146, v147, s[4:5]
	v_mul_f32_e32 v146, 0x37800000, v145
	v_cndmask_b32_e32 v145, v145, v146, vcc
	v_cmp_class_f32_e32 vcc, v144, v248
	v_fmamk_f32 v140, v240, 0x3a800000, v212
	v_mul_f32_e32 v141, 0x4f800000, v140
	v_cndmask_b32_e32 v144, v145, v144, vcc
	v_cmp_gt_f32_e32 vcc, s2, v140
	s_nop 1
	v_cndmask_b32_e32 v140, v140, v141, vcc
	v_sqrt_f32_e32 v141, v140
	s_nop 0
	v_add_u32_e32 v142, -1, v141
	v_fma_f32 v143, -v142, v141, v140
	v_cmp_ge_f32_e64 s[4:5], 0, v143
	v_add_u32_e32 v143, 1, v141
	s_nop 0
	v_cndmask_b32_e64 v142, v141, v142, s[4:5]
	v_fma_f32 v141, -v143, v141, v140
	v_cmp_lt_f32_e64 s[4:5], 0, v141
	s_nop 1
	v_cndmask_b32_e64 v141, v142, v143, s[4:5]
	v_mul_f32_e32 v142, 0x37800000, v141
	v_cndmask_b32_e32 v141, v141, v142, vcc
	v_cmp_class_f32_e32 vcc, v140, v248
	v_fmamk_f32 v136, v241, 0x3a800000, v212
	v_mul_f32_e32 v137, 0x4f800000, v136
	v_cndmask_b32_e32 v140, v141, v140, vcc
	v_cmp_gt_f32_e32 vcc, s2, v136
	s_nop 1
	v_cndmask_b32_e32 v136, v136, v137, vcc
	v_sqrt_f32_e32 v137, v136
	s_nop 0
	v_add_u32_e32 v138, -1, v137
	v_fma_f32 v139, -v138, v137, v136
	v_cmp_ge_f32_e64 s[4:5], 0, v139
	v_add_u32_e32 v139, 1, v137
	s_nop 0
	v_cndmask_b32_e64 v138, v137, v138, s[4:5]
	v_fma_f32 v137, -v139, v137, v136
	v_cmp_lt_f32_e64 s[4:5], 0, v137
	s_nop 1
	v_cndmask_b32_e64 v137, v138, v139, s[4:5]
	v_mul_f32_e32 v138, 0x37800000, v137
	v_cndmask_b32_e32 v137, v137, v138, vcc
	v_cmp_class_f32_e32 vcc, v136, v248
	v_fmamk_f32 v132, v242, 0x3a800000, v212
	v_mul_f32_e32 v133, 0x4f800000, v132
	v_cndmask_b32_e32 v136, v137, v136, vcc
	v_cmp_gt_f32_e32 vcc, s2, v132
	s_nop 1
	v_cndmask_b32_e32 v132, v132, v133, vcc
	v_sqrt_f32_e32 v133, v132
	v_rcp_f32_e32 v198, v160
	v_rcp_f32_e32 v154, v152
	v_add_u32_e32 v134, -1, v133
	v_fma_f32 v135, -v134, v133, v132
	v_cmp_ge_f32_e64 s[4:5], 0, v135
	v_add_u32_e32 v135, 1, v133
	s_nop 0
	v_cndmask_b32_e64 v134, v133, v134, s[4:5]
	v_fma_f32 v133, -v135, v133, v132
	v_cmp_lt_f32_e64 s[4:5], 0, v133
	s_nop 1
	v_cndmask_b32_e64 v133, v134, v135, s[4:5]
	v_mul_f32_e32 v134, 0x37800000, v133
	v_cndmask_b32_e32 v133, v133, v134, vcc
	v_cmp_class_f32_e32 vcc, v132, v248
	v_fmamk_f32 v128, v243, 0x3a800000, v212
	v_mul_f32_e32 v129, 0x4f800000, v128
	v_cndmask_b32_e32 v132, v133, v132, vcc
	v_cmp_gt_f32_e32 vcc, s2, v128
	v_rcp_f32_e32 v202, v148
	v_rcp_f32_e32 v200, v144
	v_cndmask_b32_e32 v128, v128, v129, vcc
	v_sqrt_f32_e32 v129, v128
	v_rcp_f32_e32 v152, v140
	v_rcp_f32_e32 v150, v136
	v_rcp_f32_e32 v148, v132
	v_add_u32_e32 v130, -1, v129
	v_fma_f32 v131, -v130, v129, v128
	v_cmp_ge_f32_e64 s[4:5], 0, v131
	v_add_u32_e32 v131, 1, v129
	s_nop 0
	v_cndmask_b32_e64 v130, v129, v130, s[4:5]
	v_fma_f32 v129, -v131, v129, v128
	v_cmp_lt_f32_e64 s[4:5], 0, v129
	s_nop 1
	v_cndmask_b32_e64 v129, v130, v131, s[4:5]
	v_mul_f32_e32 v130, 0x37800000, v129
	v_cndmask_b32_e32 v129, v129, v130, vcc
	v_cmp_class_f32_e32 vcc, v128, v248
	s_mov_b64 s[4:5], -1
	s_nop 0
	v_cndmask_b32_e32 v128, v129, v128, vcc
	v_rcp_f32_e32 v146, v128
	s_cbranch_scc1 .LBB0_726
	s_andn2_b64 vcc, exec, s[4:5]
	s_cbranch_vccz .LBB0_735
